# attention tile loops: K/mask/bias/V LDS reads issued right after the tile barrier, ahead of the next-tile LDS-DMA issue block (its temporaries renamed)
# baseline (speedup 1.0000x reference)
.LBB0_1652:
	s_or_b64 exec, exec, s[8:9]
	s_barrier
	v_cmp_le_u32_e32 vcc, s17, v97
	s_cbranch_vccz .Lmy_ma_noread
	s_lshl_b32 s10, s16, 14
	v_add3_u32 v2, s10, v93, v92
	v_add3_u32 v174, s10, v94, v92
	v_add3_u32 v175, s10, v95, v92
	v_add3_u32 v176, s10, v96, v92
	ds_read_b128 v[36:39], v2 offset:50048
	ds_read_b128 v[114:117], v174 offset:50048
	ds_read_b128 v[132:135], v175 offset:50048
	ds_read_b128 v[136:139], v176 offset:50048
	ds_read_b32 v177, v112
	ds_read2_b32 v[140:141], v113 offset0:26 offset1:27
	ds_read2_b32 v[142:143], v113 offset0:24 offset1:25
	ds_read2_b32 v[144:145], v113 offset0:18 offset1:19
	ds_read2_b32 v[146:147], v113 offset0:16 offset1:17
	ds_read2_b32 v[148:149], v113 offset0:10 offset1:11
	ds_read2_b32 v[150:151], v113 offset0:8 offset1:9
	ds_read2_b32 v[152:153], v113 offset0:2 offset1:3
	ds_read2_b32 v[154:155], v113 offset1:1
.Lmy_ma_noread:
	s_add_i32 s8, s17, 5
	v_cmp_lt_u32_e32 vcc, s8, v100
	s_and_saveexec_b64 s[8:9], vcc
	s_cbranch_execz .LBB0_1654
	s_lshl_b32 s101, s16, 14
	s_addk_i32 s101, 0xc000
	s_cmp_lg_u32 s16, 0
	s_cselect_b32 s101, s101, 0x14000
	v_add_u32_e32 v196, s101, v106
	v_add_u32_e32 v197, 0xc380, v196
	v_add_u32_e32 v196, 0xe380, v196
	v_readfirstlane_b32 s101, v197
	s_mov_b32 m0, s101
	v_readfirstlane_b32 s101, v196
	global_load_lds_dwordx4 v[88:89], off
	v_lshl_add_u64 v[198:199], s[50:51], 1, v[86:87]
	s_mov_b32 m0, s101
	s_nop 0
	global_load_lds_dwordx4 v[198:199], off
.LBB0_1654:
	s_or_b64 exec, exec, s[8:9]
	v_cmp_le_u32_e32 vcc, s17, v97
	s_and_saveexec_b64 s[8:9], vcc
	s_cbranch_execz .LBB0_1635
	s_setprio 1
	s_waitcnt lgkmcnt(12)
	v_mfma_f32_32x32x16_bf16 v[36:51], v[36:39], v[52:55], 0
	s_waitcnt lgkmcnt(11)
	v_mfma_f32_32x32x16_bf16 v[36:51], v[114:117], v[56:59], v[36:51]
	s_waitcnt lgkmcnt(10)
	v_mfma_f32_32x32x16_bf16 v[36:51], v[132:135], v[60:63], v[36:51]
	s_waitcnt lgkmcnt(9)
	v_mfma_f32_32x32x16_bf16 v[36:51], v[136:139], v[64:67], v[36:51]
	s_setprio 0
	v_add3_u32 v174, s10, v98, v107
	v_add3_u32 v175, s10, v99, v107
	ds_read_b128 v[156:159], v174 offset:58240
	ds_read_b128 v[162:165], v174 offset:60288
	ds_read_b128 v[166:169], v175 offset:58240
	ds_read_b128 v[170:173], v175 offset:60288
	s_waitcnt lgkmcnt(4)
	v_lshrrev_b32_e32 v2, v102, v177
	v_bfe_i32 v178, v2, 0, 1
	v_bfe_i32 v179, v2, 1, 1
	v_bfe_i32 v180, v2, 2, 1
	v_bfe_i32 v181, v2, 3, 1
	v_bfe_i32 v182, v2, 8, 1
	v_bfe_i32 v183, v2, 9, 1
	v_bfe_i32 v184, v2, 10, 1
	v_bfe_i32 v185, v2, 11, 1
	v_bfe_i32 v186, v2, 16, 1
	v_bfe_i32 v187, v2, 17, 1
	v_bfe_i32 v188, v2, 18, 1
	v_bfe_i32 v189, v2, 19, 1
	v_bfe_i32 v190, v2, 24, 1
	v_bfe_i32 v191, v2, 25, 1
	v_bfe_i32 v192, v2, 26, 1
	v_bfe_i32 v193, v2, 27, 1
	v_pk_fma_f32 v[36:37], v[36:37], s[82:83], v[140:141] op_sel:[0,0,1] op_sel_hi:[1,0,0]
	v_pk_fma_f32 v[38:39], v[38:39], s[82:83], v[142:143] op_sel:[0,0,1] op_sel_hi:[1,0,0]
	v_bfi_b32 v36, v178, v36, v228
	v_bfi_b32 v37, v179, v37, v228
	v_bfi_b32 v38, v180, v38, v228
	v_bfi_b32 v39, v181, v39, v228
	v_max_f32_e32 v116, v36, v37
	v_max_f32_e32 v114, v38, v39
	v_max3_f32 v116, v116, s90, v114
	v_pk_fma_f32 v[40:41], v[40:41], s[82:83], v[144:145] op_sel:[0,0,1] op_sel_hi:[1,0,0]
	v_pk_fma_f32 v[42:43], v[42:43], s[82:83], v[146:147] op_sel:[0,0,1] op_sel_hi:[1,0,0]
	v_bfi_b32 v40, v182, v40, v228
	v_bfi_b32 v41, v183, v41, v228
	v_bfi_b32 v42, v184, v42, v228
	v_bfi_b32 v43, v185, v43, v228
	v_max_f32_e32 v117, v40, v41
	v_max_f32_e32 v114, v42, v43
	v_max3_f32 v116, v116, v117, v114
	v_pk_fma_f32 v[44:45], v[44:45], s[82:83], v[148:149] op_sel:[0,0,1] op_sel_hi:[1,0,0]
	v_pk_fma_f32 v[46:47], v[46:47], s[82:83], v[150:151] op_sel:[0,0,1] op_sel_hi:[1,0,0]
	v_bfi_b32 v44, v186, v44, v228
	v_bfi_b32 v45, v187, v45, v228
	v_bfi_b32 v46, v188, v46, v228
	v_bfi_b32 v47, v189, v47, v228
	v_max_f32_e32 v117, v44, v45
	v_max_f32_e32 v114, v46, v47
	v_max3_f32 v116, v116, v117, v114
	v_pk_fma_f32 v[48:49], v[48:49], s[82:83], v[152:153] op_sel:[0,0,1] op_sel_hi:[1,0,0]
	v_pk_fma_f32 v[50:51], v[50:51], s[82:83], v[154:155] op_sel:[0,0,1] op_sel_hi:[1,0,0]
	v_bfi_b32 v48, v190, v48, v228
	v_bfi_b32 v49, v191, v49, v228
	v_bfi_b32 v50, v192, v50, v228
	v_bfi_b32 v51, v193, v51, v228
	v_max_f32_e32 v117, v48, v49
	v_max_f32_e32 v2, v50, v51
	v_max3_f32 v2, v116, v117, v2
	v_mov_b32_e32 v114, v2
	v_mov_b32_e32 v115, v2
	s_nop 1
	v_permlane32_swap_b32_e32 v114, v115
	v_max3_f32 v2, v2, v114, v115
	v_add_f32_e32 v114, 0x41000000, v90
	v_cmp_gt_f32_e32 vcc, v2, v114
	s_cbranch_vccz .LBB0_1634
	v_max_f32_e32 v2, v2, v2
	v_max_f32_e32 v114, v90, v90
	v_max_f32_e32 v114, v114, v2
	v_sub_f32_e32 v2, v90, v114
	v_exp_f32_e32 v2, v2
	v_mov_b32_e32 v90, v114
	v_pk_mul_f32 v[34:35], v[34:35], v[2:3] op_sel_hi:[1,0]
	v_pk_mul_f32 v[32:33], v[32:33], v[2:3] op_sel_hi:[1,0]
	v_pk_mul_f32 v[30:31], v[30:31], v[2:3] op_sel_hi:[1,0]
	v_pk_mul_f32 v[28:29], v[28:29], v[2:3] op_sel_hi:[1,0]
	v_pk_mul_f32 v[26:27], v[26:27], v[2:3] op_sel_hi:[1,0]
	v_pk_mul_f32 v[24:25], v[24:25], v[2:3] op_sel_hi:[1,0]
	v_pk_mul_f32 v[22:23], v[22:23], v[2:3] op_sel_hi:[1,0]
	v_pk_mul_f32 v[20:21], v[20:21], v[2:3] op_sel_hi:[1,0]
	v_pk_mul_f32 v[18:19], v[18:19], v[2:3] op_sel_hi:[1,0]
	v_pk_mul_f32 v[16:17], v[16:17], v[2:3] op_sel_hi:[1,0]
	v_pk_mul_f32 v[14:15], v[14:15], v[2:3] op_sel_hi:[1,0]
	v_pk_mul_f32 v[12:13], v[12:13], v[2:3] op_sel_hi:[1,0]
	v_pk_mul_f32 v[10:11], v[10:11], v[2:3] op_sel_hi:[1,0]
	v_pk_mul_f32 v[8:9], v[8:9], v[2:3] op_sel_hi:[1,0]
	v_pk_mul_f32 v[6:7], v[6:7], v[2:3] op_sel_hi:[1,0]
	v_pk_mul_f32 v[4:5], v[4:5], v[2:3] op_sel_hi:[1,0]
	v_mul_f32_e32 v110, v110, v2
	s_branch .LBB0_1634

.LBB0_1707:
	s_or_b64 exec, exec, s[34:35]
	s_barrier
	v_cmp_le_u32_e32 vcc, s49, v144
	s_cbranch_vccz .Lmy_dl_noread
	s_lshl_b32 s38, s46, 14
	v_add3_u32 v2, s38, v140, v139
	v_add3_u32 v202, s38, v141, v139
	v_add3_u32 v203, s38, v142, v139
	v_add3_u32 v204, s38, v143, v139
	ds_read_b128 v[36:39], v2 offset:16640
	ds_read_b128 v[52:55], v202 offset:16640
	ds_read_b128 v[178:181], v203 offset:16640
	ds_read_b128 v[182:185], v204 offset:16640
	v_add3_u32 v202, s38, v145, v152
	v_add3_u32 v203, s38, v146, v152
	ds_read_b128 v[186:189], v202 offset:24832
	ds_read_b128 v[190:193], v202 offset:26880
	ds_read_b128 v[194:197], v203 offset:24832
	ds_read_b128 v[198:201], v203 offset:26880
.Lmy_dl_noread:
	s_add_i32 s34, s49, 5
	v_cmp_lt_u32_e32 vcc, s34, v147
	s_and_saveexec_b64 s[34:35], vcc
	s_cbranch_execz .LBB0_1709
	s_lshl_b32 s36, s46, 14
	s_addk_i32 s36, 0xc000
	s_cmp_lg_u32 s46, 0
	s_cselect_b32 s36, s36, 0x14000
	v_add_u32_e32 v237, s36, v151
	v_add_u32_e32 v238, 0x4100, v237
	v_add_u32_e32 v237, 0x6100, v237
	v_readfirstlane_b32 s36, v238
	s_mov_b32 m0, s36
	s_add_i32 s50, s47, 0xfffffe81
	v_readfirstlane_b32 s36, v237
	global_load_lds_dwordx4 v[128:129], off
	v_lshl_add_u64 v[240:241], s[50:51], 1, v[126:127]
	s_mov_b32 m0, s36
	s_nop 0
	global_load_lds_dwordx4 v[240:241], off
.LBB0_1709:
	s_or_b64 exec, exec, s[34:35]
	v_cmp_le_u32_e32 vcc, s49, v144
	s_and_saveexec_b64 s[34:35], vcc
	s_cbranch_execz .LBB0_1690
	s_setprio 1
	s_waitcnt lgkmcnt(7)
	v_mfma_f32_32x32x16_bf16 v[36:51], v[36:39], v[92:95], 0
	s_waitcnt lgkmcnt(6)
	v_mfma_f32_32x32x16_bf16 v[36:51], v[52:55], v[96:99], v[36:51]
	s_waitcnt lgkmcnt(5)
	v_mfma_f32_32x32x16_bf16 v[36:51], v[178:181], v[100:103], v[36:51]
	s_waitcnt lgkmcnt(4)
	v_mfma_f32_32x32x16_bf16 v[36:51], v[182:185], v[104:107], v[36:51]
	s_setprio 0
	s_mov_b64 s[36:37], -1
	s_cmp_ge_i32 s47, s42
	v_add_f32_e32 v159, 0x41000000, v158
	s_cbranch_scc0 .LBB0_1714
	v_add_u32_e32 v2, 0x1e7c, v156
	v_add_u32_e32 v205, 0x1e74, v156
	v_add_u32_e32 v56, 0x1e5c, v156
	v_add_u32_e32 v58, 0x1e54, v156
	ds_read2_b32 v[52:53], v2 offset1:1
	ds_read2_b32 v[54:55], v205 offset1:1
	ds_read2_b32 v[56:57], v56 offset1:1
	ds_read2_b32 v[58:59], v58 offset1:1
	v_add_u32_e32 v2, 0x1e3c, v156
	v_add_u32_e32 v205, 0x1e34, v156
	v_add_u32_e32 v235, 0x1e1c, v156
	v_add_u32_e32 v236, 0x1e14, v156
	ds_read2_b32 v[206:207], v2 offset1:1
	ds_read2_b32 v[208:209], v205 offset1:1
	ds_read2_b32 v[210:211], v235 offset1:1
	ds_read2_b32 v[212:213], v236 offset1:1
	s_waitcnt lgkmcnt(4)
	v_pk_fma_f32 v[130:131], v[36:37], s[82:83], v[52:53] op_sel:[0,0,1] op_sel_hi:[1,0,0]
	v_pk_fma_f32 v[88:89], v[38:39], s[82:83], v[54:55] op_sel:[0,0,1] op_sel_hi:[1,0,0]
	v_max_f32_e32 v2, v130, v131
	v_max_f32_e32 v52, v88, v89
	v_pk_fma_f32 v[86:87], v[40:41], s[82:83], v[56:57] op_sel:[0,0,1] op_sel_hi:[1,0,0]
	v_pk_fma_f32 v[84:85], v[42:43], s[82:83], v[58:59] op_sel:[0,0,1] op_sel_hi:[1,0,0]
	v_max3_f32 v2, v2, s90, v52
	v_max_f32_e32 v52, v86, v87
	v_max_f32_e32 v53, v84, v85
	v_max3_f32 v2, v2, v52, v53
	s_waitcnt lgkmcnt(0)
	v_pk_fma_f32 v[136:137], v[44:45], s[82:83], v[206:207] op_sel:[0,0,1] op_sel_hi:[1,0,0]
	v_mov_b32_e32 v160, v157
	v_pk_fma_f32 v[134:135], v[46:47], s[82:83], v[208:209] op_sel:[0,0,1] op_sel_hi:[1,0,0]
	v_max_f32_e32 v52, v136, v137
	v_max_f32_e32 v53, v134, v135
	v_pk_fma_f32 v[132:133], v[48:49], s[82:83], v[210:211] op_sel:[0,0,1] op_sel_hi:[1,0,0]
	v_pk_fma_f32 v[90:91], v[50:51], s[82:83], v[212:213] op_sel:[0,0,1] op_sel_hi:[1,0,0]
	v_max3_f32 v2, v2, v52, v53
	v_max_f32_e32 v52, v132, v133
	v_max_f32_e32 v53, v90, v91
	v_max3_f32 v2, v2, v52, v53
	v_mov_b32_e32 v52, v2
	v_mov_b32_e32 v53, v2
	s_nop 1
	v_permlane32_swap_b32_e32 v52, v53
	v_max3_f32 v161, v2, v52, v53
	v_cmp_gt_f32_e32 vcc, v161, v159
	v_mov_b32_e32 v2, v158
	s_cbranch_vccz .LBB0_1713
	v_max_f32_e32 v2, v161, v161
	v_max_f32_e32 v52, v158, v158
	v_max_f32_e32 v2, v52, v2
	v_sub_f32_e32 v52, v158, v2
	v_exp_f32_e32 v160, v52
	s_nop 0
	v_pk_mul_f32 v[34:35], v[34:35], v[160:161] op_sel_hi:[1,0]
	v_pk_mul_f32 v[32:33], v[32:33], v[160:161] op_sel_hi:[1,0]
	v_pk_mul_f32 v[30:31], v[30:31], v[160:161] op_sel_hi:[1,0]
	v_pk_mul_f32 v[28:29], v[28:29], v[160:161] op_sel_hi:[1,0]
	v_pk_mul_f32 v[26:27], v[26:27], v[160:161] op_sel_hi:[1,0]
	v_pk_mul_f32 v[24:25], v[24:25], v[160:161] op_sel_hi:[1,0]
	v_pk_mul_f32 v[22:23], v[22:23], v[160:161] op_sel_hi:[1,0]
	v_pk_mul_f32 v[20:21], v[20:21], v[160:161] op_sel_hi:[1,0]
	v_pk_mul_f32 v[18:19], v[18:19], v[160:161] op_sel_hi:[1,0]
	v_pk_mul_f32 v[16:17], v[16:17], v[160:161] op_sel_hi:[1,0]
	v_pk_mul_f32 v[14:15], v[14:15], v[160:161] op_sel_hi:[1,0]
	v_pk_mul_f32 v[12:13], v[12:13], v[160:161] op_sel_hi:[1,0]
	v_pk_mul_f32 v[10:11], v[10:11], v[160:161] op_sel_hi:[1,0]
	v_pk_mul_f32 v[8:9], v[8:9], v[160:161] op_sel_hi:[1,0]
	v_pk_mul_f32 v[6:7], v[6:7], v[160:161] op_sel_hi:[1,0]
	v_pk_mul_f32 v[4:5], v[4:5], v[160:161] op_sel_hi:[1,0]
	v_mul_f32_e32 v160, v157, v160
